# as v43 plus attention odd-tile load addresses from the even-tile pointers plus a constant (no 64-bit multiply-adds in the loop)
# speedup vs baseline: 1.0139x; 1.0014x over previous
.LBB0_967:
	s_or_b64 exec, exec, s[18:19]
	v_add_f32_e32 v80, v154, v155
	v_fmamk_f32 v80, v80, 0x3c2aaaab, v210
	v_mul_f32_e32 v81, 0x4b800000, v80
	v_cmp_gt_f32_e32 vcc, s56, v80
	s_mov_b32 s18, 0x3e16c740
	s_lshl_b32 s25, s25, 2
	v_cndmask_b32_e32 v80, v80, v81, vcc
	v_rsq_f32_e32 v80, v80
	s_add_i32 s26, s25, 4
	s_mov_b32 s30, 0
	v_lshl_add_u64 v[202:203], v[166:167], 1, s[16:17]
	v_mul_f32_e32 v81, 0x45800000, v80
	v_cndmask_b32_e32 v80, v80, v81, vcc
	v_mul_f32_e32 v82, 0x3e16c740, v80
	s_waitcnt vmcnt(10)
	v_pk_mul_f32 v[52:53], v[52:53], v[82:83] op_sel_hi:[1,0]
	v_pk_mul_f32 v[88:89], v[88:89], v[82:83] op_sel_hi:[1,0]
	v_pk_mul_f32 v[52:53], v[52:53], v[124:125]
	v_pk_mul_f32 v[90:91], v[90:91], v[82:83] op_sel_hi:[1,0]
	v_cvt_pk_bf16_f32 v102, v52, v53
	v_pk_mul_f32 v[52:53], v[80:81], v[106:107] op_sel_hi:[0,1]
	global_load_dwordx4 v[104:107], v[198:199], off offset:256
	s_waitcnt vmcnt(8)
	v_pk_mul_f32 v[36:37], v[36:37], v[52:53]
	v_pk_mul_f32 v[52:53], v[80:81], v[120:121] op_sel_hi:[0,1]
	s_waitcnt vmcnt(6)
	v_pk_mul_f32 v[32:33], v[52:53], v[32:33]
	v_pk_mul_f32 v[76:77], v[76:77], v[82:83] op_sel_hi:[1,0]
	s_waitcnt vmcnt(2)
	v_pk_mul_f32 v[52:53], v[44:45], v[32:33]
	v_pk_mul_f32 v[32:33], v[40:41], v[32:33]
	v_pk_fma_f32 v[52:53], v[40:41], v[36:37], v[52:53] neg_lo:[0,0,1] neg_hi:[0,0,1]
	v_pk_fma_f32 v[32:33], v[44:45], v[36:37], v[32:33]
	v_pk_mul_f32 v[36:37], v[80:81], v[116:117] op_sel_hi:[0,1]
	v_pk_mul_f32 v[36:37], v[38:39], v[36:37]
	v_pk_mul_f32 v[38:39], v[80:81], v[118:119] op_sel_hi:[0,1]
	v_pk_mul_f32 v[34:35], v[38:39], v[34:35]
	v_pk_mul_f32 v[32:33], v[32:33], s[18:19] op_sel_hi:[1,0]
	v_pk_mul_f32 v[38:39], v[46:47], v[34:35]
	v_pk_mul_f32 v[34:35], v[42:43], v[34:35]
	v_pk_fma_f32 v[38:39], v[42:43], v[36:37], v[38:39] neg_lo:[0,0,1] neg_hi:[0,0,1]
	v_pk_fma_f32 v[34:35], v[46:47], v[36:37], v[34:35]
	v_pk_mul_f32 v[36:37], v[80:81], v[112:113] op_sel_hi:[0,1]
	v_pk_mul_f32 v[16:17], v[36:37], v[16:17]
	v_pk_mul_f32 v[36:37], v[80:81], v[114:115] op_sel_hi:[0,1]
	v_pk_mul_f32 v[20:21], v[36:37], v[20:21]
	v_cvt_pk_bf16_f32 v112, v32, v33
	v_pk_mul_f32 v[36:37], v[28:29], v[20:21]
	v_pk_mul_f32 v[20:21], v[24:25], v[20:21]
	v_pk_fma_f32 v[36:37], v[24:25], v[16:17], v[36:37] neg_lo:[0,0,1] neg_hi:[0,0,1]
	v_pk_fma_f32 v[16:17], v[28:29], v[16:17], v[20:21]
	v_pk_mul_f32 v[20:21], v[80:81], v[108:109] op_sel_hi:[0,1]
	v_pk_mul_f32 v[18:19], v[20:21], v[18:19]
	v_pk_mul_f32 v[20:21], v[80:81], v[110:111] op_sel_hi:[0,1]
	v_pk_mul_f32 v[20:21], v[20:21], v[22:23]
	v_mov_b32_e32 v32, v209
	v_pk_mul_f32 v[22:23], v[30:31], v[20:21]
	v_pk_mul_f32 v[20:21], v[26:27], v[20:21]
	v_pk_fma_f32 v[22:23], v[26:27], v[18:19], v[22:23] neg_lo:[0,0,1] neg_hi:[0,0,1]
	v_pk_fma_f32 v[18:19], v[30:31], v[18:19], v[20:21]
	v_pk_mul_f32 v[78:79], v[78:79], v[82:83] op_sel_hi:[1,0]
	v_pk_mul_f32 v[72:73], v[72:73], v[82:83] op_sel_hi:[1,0]
	v_pk_mul_f32 v[74:75], v[74:75], v[82:83] op_sel_hi:[1,0]
	v_pk_mul_f32 v[68:69], v[68:69], v[82:83] op_sel_hi:[1,0]
	v_pk_mul_f32 v[70:71], v[70:71], v[82:83] op_sel_hi:[1,0]
	v_pk_mul_f32 v[64:65], v[64:65], v[82:83] op_sel_hi:[1,0]
	v_pk_mul_f32 v[66:67], v[66:67], v[82:83] op_sel_hi:[1,0]
	v_pk_mul_f32 v[60:61], v[60:61], v[82:83] op_sel_hi:[1,0]
	v_pk_mul_f32 v[62:63], v[62:63], v[82:83] op_sel_hi:[1,0]
	v_pk_mul_f32 v[56:57], v[56:57], v[82:83] op_sel_hi:[1,0]
	v_pk_mul_f32 v[58:59], v[58:59], v[82:83] op_sel_hi:[1,0]
	v_pk_mul_f32 v[54:55], v[54:55], v[82:83] op_sel_hi:[1,0]
	v_pk_mul_f32 v[38:39], v[38:39], s[18:19] op_sel_hi:[1,0]
	v_pk_mul_f32 v[34:35], v[34:35], s[18:19] op_sel_hi:[1,0]
	v_pk_mul_f32 v[36:37], v[36:37], s[18:19] op_sel_hi:[1,0]
	v_pk_mul_f32 v[16:17], v[16:17], s[18:19] op_sel_hi:[1,0]
	v_pk_mul_f32 v[22:23], v[22:23], s[18:19] op_sel_hi:[1,0]
	v_pk_mul_f32 v[18:19], v[18:19], s[18:19] op_sel_hi:[1,0]
	s_waitcnt lgkmcnt(0)
	s_barrier
	v_pk_mul_f32 v[88:89], v[88:89], v[152:153]
	v_mov_b32_e32 v33, v32
	v_pk_mul_f32 v[90:91], v[90:91], v[150:151]
	v_pk_mul_f32 v[76:77], v[76:77], v[148:149]
	v_pk_mul_f32 v[78:79], v[78:79], v[146:147]
	v_pk_mul_f32 v[72:73], v[72:73], v[144:145]
	v_pk_mul_f32 v[74:75], v[74:75], v[142:143]
	v_pk_mul_f32 v[68:69], v[68:69], v[140:141]
	v_pk_mul_f32 v[70:71], v[70:71], v[138:139]
	v_pk_mul_f32 v[64:65], v[64:65], v[136:137]
	v_pk_mul_f32 v[66:67], v[66:67], v[134:135]
	v_pk_mul_f32 v[60:61], v[60:61], v[132:133]
	v_pk_mul_f32 v[62:63], v[62:63], v[130:131]
	v_pk_mul_f32 v[56:57], v[56:57], v[128:129]
	v_pk_mul_f32 v[58:59], v[58:59], v[126:127]
	v_pk_mul_f32 v[54:55], v[54:55], v[122:123]
	v_pk_mul_f32 v[52:53], v[52:53], s[18:19] op_sel_hi:[1,0]
	v_cvt_pk_bf16_f32 v109, v38, v39
	v_cvt_pk_bf16_f32 v110, v36, v37
	v_cvt_pk_bf16_f32 v111, v22, v23
	v_cvt_pk_bf16_f32 v113, v34, v35
	v_cvt_pk_bf16_f32 v114, v16, v17
	v_cvt_pk_bf16_f32 v115, v18, v19
	v_mov_b32_e32 v34, v32
	v_mov_b32_e32 v35, v32
	v_mov_b32_e32 v36, v32
	v_mov_b32_e32 v37, v32
	v_mov_b32_e32 v38, v32
	v_mov_b32_e32 v39, v32
	v_mov_b32_e32 v40, v32
	v_mov_b32_e32 v41, v32
	v_mov_b32_e32 v42, v32
	v_mov_b32_e32 v43, v32
	v_mov_b32_e32 v44, v32
	v_mov_b32_e32 v45, v32
	v_mov_b32_e32 v46, v32
	v_mov_b32_e32 v47, v32
	v_mov_b64_e32 v[16:17], v[32:33]
	s_waitcnt vmcnt(1)
	v_mov_b64_e32 v[82:83], v[50:51]
	v_cvt_pk_bf16_f32 v88, v88, v89
	v_cvt_pk_bf16_f32 v89, v90, v91
	v_cvt_pk_bf16_f32 v90, v76, v77
	v_cvt_pk_bf16_f32 v91, v78, v79
	v_cvt_pk_bf16_f32 v92, v72, v73
	v_cvt_pk_bf16_f32 v93, v74, v75
	v_cvt_pk_bf16_f32 v94, v68, v69
	v_cvt_pk_bf16_f32 v95, v70, v71
	v_cvt_pk_bf16_f32 v96, v64, v65
	v_cvt_pk_bf16_f32 v97, v66, v67
	v_cvt_pk_bf16_f32 v98, v60, v61
	v_cvt_pk_bf16_f32 v99, v62, v63
	v_cvt_pk_bf16_f32 v100, v56, v57
	v_cvt_pk_bf16_f32 v101, v58, v59
	v_cvt_pk_bf16_f32 v103, v54, v55
	v_cvt_pk_bf16_f32 v108, v52, v53
	s_or_b32 s27, s24, 31
	v_lshl_add_u64 v[204:205], v[170:171], 1, s[16:17]
	v_or_b32_e32 v223, s24, v160
	v_lshl_add_u64 v[206:207], v[192:193], 0, s[64:65]
	v_lshl_add_u64 v[216:217], v[194:195], 0, s[14:15]
	v_lshl_add_u64 v[218:219], v[196:197], 0, s[14:15]
	v_mov_b32_e32 v173, 0
	s_movk_i32 s28, 0x7f
	v_mov_b64_e32 v[18:19], v[34:35]
	v_mov_b64_e32 v[20:21], v[36:37]
	v_mov_b64_e32 v[22:23], v[38:39]
	v_mov_b64_e32 v[24:25], v[40:41]
	v_mov_b64_e32 v[26:27], v[42:43]
	v_mov_b64_e32 v[28:29], v[44:45]
	v_mov_b64_e32 v[30:31], v[46:47]
	v_mov_b64_e32 v[80:81], v[48:49]
	s_mov_b64 s[34:35], 0x3000

.LBB0_980:
	s_waitcnt lgkmcnt(0)
	s_barrier
	s_waitcnt vmcnt(0)
	s_cmp_ge_u32 s30, s25
	s_cbranch_scc1 .LBB0_985
	v_lshl_add_u64 v[50:51], v[218:219], 0, s[34:35]
	global_load_dwordx4 v[84:87], v[50:51], off
	s_and_saveexec_b64 s[18:19], s[2:3]
	s_cbranch_execz .LBB0_983
	v_lshl_add_u64 v[50:51], v[216:217], 0, s[34:35]
	global_load_dwordx4 v[80:83], v[50:51], off
.LBB0_983:
	s_or_b64 exec, exec, s[18:19]
	global_load_dwordx4 v[104:107], v[206:207], off offset:128
	s_sub_i32 s16, s28, 63
	s_cmp_gt_i32 s16, s27
	s_cbranch_scc0 .LBB0_986
